# speedup vs baseline: 1.0258x; 1.0186x over previous
.Lnoprio:
	s_xor_b64 s[4:5], s[10:11], -1
	s_lshl_b64 s[28:29], s[24:25], 16
	s_cmp_eq_u64 vcc, s[12:13]
	s_cselect_b64 s[12:13], -1, 0
	s_and_b64 s[20:21], s[12:13], s[4:5]
	s_add_u32 s33, s16, s28
	s_addc_u32 s35, s17, s29
	s_mul_i32 s40, s6, s7
	s_ashr_i32 s7, s6, 31
	s_sub_i32 s41, s24, s40
	s_lshl_b64 s[4:5], s[6:7], 23
	s_add_u32 s4, s8, s4
	s_addc_u32 s5, s9, s5
	s_lshl_b32 s8, s34, 8
	s_lshl_b32 s9, s34, 10
	s_add_u32 s28, s4, s9
	s_addc_u32 s29, s5, 0
	s_lshl_b64 s[4:5], s[6:7], 21
	s_add_u32 s4, s14, s4
	s_addc_u32 s5, s15, s5
	s_lshl_b32 s42, s34, 6
	s_add_u32 s30, s4, s8
	s_addc_u32 s31, s5, 0
	v_and_b32_e32 v171, 15, v162
	s_lshl_b32 s4, s41, 6
	v_lshl_or_b32 v130, v171, 2, s4
	v_subrev_u32_e32 v201, 32, v130
	v_max_i32_e32 v130, 0, v201
	v_sub_u32_e32 v131, 0x7ff, v130
	v_cndmask_b32_e64 v130, v131, v130, s[0:1]
	v_bfe_u32 v146, v162, 4, 2
	v_ashrrev_i32_e32 v131, 31, v130
	v_or_b32_e32 v199, v137, v146
	v_lshlrev_b64 v[130:131], 12, v[130:131]
	v_or_b32_e32 v134, 4, v199
	v_lshl_add_u64 v[130:131], s[28:29], 0, v[130:131]
	v_mov_b32_e32 v167, 0
	v_lshlrev_b32_e32 v166, 4, v199
	v_lshl_add_u64 v[132:133], v[130:131], 0, v[166:167]
	v_lshlrev_b32_e32 v166, 4, v134
	v_lshl_add_u64 v[130:131], v[130:131], 0, v[166:167]
	global_load_dwordx4 v[142:145], v[130:131], off
	global_load_dwordx4 v[138:141], v[132:133], off
	v_lshlrev_b32_e32 v164, 2, v199
	v_lshlrev_b32_e32 v170, 2, v134
	v_lshlrev_b32_e32 v134, 8, v171
	s_mov_b32 s4, 0x8400
	v_add3_u32 v203, v134, v164, s4
	v_lshlrev_b32_e32 v134, 1, v1
	v_sub_u32_e32 v135, v134, v171
	v_or_b32_e32 v134, 1, v134
	v_sub_u32_e32 v134, v134, v171
	s_lshl_b32 s4, s34, 4
	v_lshlrev_b32_e32 v206, 2, v134
	v_mul_u32_u24_e32 v134, 6, v1
	s_add_i32 s4, s4, 16
	v_mad_u32_u24 v130, v1, 6, s4
	v_and_b32_e32 v131, 14, v134
	v_and_or_b32 v130, v130, 48, v131
	v_lshlrev_b32_e32 v172, 6, v130
	v_or_b32_e32 v130, 1, v134
	v_add_u32_e32 v130, s4, v130
	v_bitop3_b32 v131, v134, 15, 1 bitop3:0xc8
	v_and_or_b32 v130, v130, 48, v131
	v_lshlrev_b32_e32 v174, 6, v130
	v_mad_u32_u24 v130, v1, 6, 2
	v_add_u32_e32 v131, s4, v130
	v_and_b32_e32 v132, 14, v130
	v_and_or_b32 v131, v131, 48, v132
	v_lshlrev_b32_e32 v176, 6, v131
	v_mad_u32_u24 v131, v1, 6, 3
	v_and_b32_e32 v136, 63, v162
	v_add_u32_e32 v132, s4, v131
	v_and_b32_e32 v133, 15, v131
	v_lshlrev_b32_e32 v166, 2, v136
	v_and_or_b32 v132, v132, 48, v133
	v_lshlrev_b32_e32 v204, 2, v135
	v_lshl_or_b32 v135, v1, 9, v166
	v_lshlrev_b32_e32 v178, 6, v132
	v_mad_u32_u24 v132, v1, 6, 4
	v_add_u32_e32 v205, 0x8400, v135
	v_add_u32_e32 v133, s4, v132
	v_and_b32_e32 v135, 14, v132
	v_and_or_b32 v133, v133, 48, v135
	s_add_i32 s34, s34, 1
	v_lshrrev_b32_e32 v134, 4, v134
	v_lshl_add_u32 v184, v1, 7, s9
	v_lshlrev_b32_e32 v180, 6, v133
	v_mad_u32_u24 v133, v1, 6, 5
	v_add_lshl_u32 v134, s34, v134, 6
	v_mul_u32_u24_e32 v1, 24, v1
	v_and_b32_e32 v134, 0xc0, v134
	v_and_b32_e32 v1, 56, v1
	v_or3_b32 v183, v1, v134, v146
	v_lshrrev_b32_e32 v1, 4, v130
	v_add_lshl_u32 v1, s34, v1, 6
	v_lshlrev_b32_e32 v130, 2, v130
	v_and_b32_e32 v1, 0xc0, v1
	v_and_b32_e32 v130, 56, v130
	v_or3_b32 v185, v130, v1, v146
	v_lshrrev_b32_e32 v1, 4, v131
	v_add_lshl_u32 v1, s34, v1, 6
	v_lshlrev_b32_e32 v130, 2, v131
	v_and_b32_e32 v1, 0xc0, v1
	v_and_b32_e32 v130, 60, v130
	v_or3_b32 v192, v130, v1, v146
	v_lshrrev_b32_e32 v1, 4, v132
	v_add_lshl_u32 v1, s34, v1, 6
	v_lshlrev_b32_e32 v130, 2, v132
	v_and_b32_e32 v1, 0xc0, v1
	v_and_b32_e32 v130, 56, v130
	v_or3_b32 v193, v130, v1, v146
	v_lshrrev_b32_e32 v1, 4, v133
	v_add_u32_e32 v135, s4, v133
	v_and_b32_e32 v137, 15, v133
	v_add_lshl_u32 v1, s34, v1, 6
	v_lshlrev_b32_e32 v130, 2, v133
	v_and_or_b32 v135, v135, 48, v137
	v_and_b32_e32 v1, 0xc0, v1
	v_and_b32_e32 v130, 60, v130
	v_lshlrev_b32_e32 v182, 6, v135
	v_or3_b32 v194, v130, v1, v146
	v_lshlrev_b32_e32 v168, 3, v136
	s_waitcnt vmcnt(1)
	v_mov_b64_e32 v[130:131], v[142:143]
	s_waitcnt vmcnt(0)
	v_mov_b64_e32 v[134:135], v[138:139]
	s_mov_b32 s43, 0
	v_lshlrev_b32_e32 v173, 3, v146
	v_and_b32_e32 v200, 48, v162
	v_add_u32_e32 v181, s42, v199
	s_mov_b32 s34, 0x48800000
	s_mov_b32 s36, 0x36800000
	v_mov_b32_e32 v188, v167
	v_mov_b32_e32 v189, v167
	v_mul_u32_u24_e32 v195, 0x210, v171
	v_bfe_u32 v216, v162, 4, 1
	v_bfe_u32 v217, v162, 5, 1
	s_lshr_b32 s4, s42, 6
	s_add_i32 s4, s4, 1
	v_lshlrev_b32_e32 v218, 3, v171
	v_lshrrev_b32_e32 v219, 6, v162
	v_mad_u32_u24 v219, v219, 6, v217
	v_lshrrev_b32_e32 v220, 4, v219
	v_add_u32_e32 v220, s4, v220
	v_and_b32_e32 v220, 3, v220
	v_and_b32_e32 v221, 15, v219
	v_lshl_add_u32 v222, v220, 4, v221
	v_lshlrev_b32_e32 v223, 6, v222
	v_lshl_add_u32 v223, v216, 1, v223
	v_lshl_add_u32 v223, v171, 2, v223
	v_lshlrev_b32_e32 v228, 3, v223
	v_lshlrev_b32_e32 v223, 2, v222
	v_lshl_add_u32 v223, v216, 1, v223
	v_lshl_add_u32 v231, v223, 1, v195
	v_add_u32_e32 v219, 2, v219
	v_lshrrev_b32_e32 v220, 4, v219
	v_add_u32_e32 v220, s4, v220
	v_and_b32_e32 v220, 3, v220
	v_and_b32_e32 v221, 15, v219
	v_lshl_add_u32 v222, v220, 4, v221
	v_lshlrev_b32_e32 v223, 6, v222
	v_lshl_add_u32 v223, v216, 1, v223
	v_lshl_add_u32 v223, v171, 2, v223
	v_lshlrev_b32_e32 v229, 3, v223
	v_lshlrev_b32_e32 v223, 2, v222
	v_lshl_add_u32 v223, v216, 1, v223
	v_lshl_add_u32 v232, v223, 1, v195
	v_add_u32_e32 v219, 2, v219
	v_lshrrev_b32_e32 v220, 4, v219
	v_add_u32_e32 v220, s4, v220
	v_and_b32_e32 v220, 3, v220
	v_and_b32_e32 v221, 15, v219
	v_lshl_add_u32 v222, v220, 4, v221
	v_lshlrev_b32_e32 v223, 6, v222
	v_lshl_add_u32 v223, v216, 1, v223
	v_lshl_add_u32 v223, v171, 2, v223
	v_lshlrev_b32_e32 v230, 3, v223
	v_lshlrev_b32_e32 v223, 2, v222
	v_lshl_add_u32 v223, v216, 1, v223
	v_lshl_add_u32 v233, v223, 1, v195
	v_and_b32_e32 v219, 15, v162
	v_bfe_u32 v220, v162, 4, 2
	v_lshl_add_u32 v219, v219, 2, v220
	v_lshlrev_b32_e32 v219, 3, v219
	v_lshl_add_u32 v234, v184, 3, v219
	v_mov_b32_e32 v207, 1
	v_mov_b32_e32 v202, 0
	v_mov_b32_e32 v198, 0
	v_mov_b32_e32 v197, 0
	v_mov_b32_e32 v196, 0
	v_mov_b32_e32 v179, 0
	v_mov_b32_e32 v177, 0
	v_mov_b32_e32 v175, 0
	v_mov_b32_e32 v1, 0
	v_lshl_add_u64 v[186:187], s[30:31], 0, v[166:167]
	v_mov_b64_e32 v[132:133], v[144:145]
	v_mov_b64_e32 v[136:137], v[140:141]

.LBB1_38:
	global_load_dwordx4 v[140:143], v228, s[52:53] sc1
	global_load_dwordx4 v[144:147], v229, s[52:53] sc1
	global_load_dwordx4 v[148:151], v230, s[52:53] sc1
	s_waitcnt vmcnt(2)
	v_cmp_eq_u32_e32 vcc, s44, v141
	v_cmp_eq_u32_e64 s[6:7], s44, v143
	s_waitcnt vmcnt(1)
	v_cmp_eq_u32_e64 s[8:9], s44, v145
	s_and_b64 s[6:7], vcc, s[6:7]
	v_cmp_eq_u32_e64 s[10:11], s44, v147
	s_and_b64 s[6:7], s[6:7], s[8:9]
	s_waitcnt vmcnt(0)
	v_cmp_eq_u32_e64 s[12:13], s44, v149
	s_and_b64 s[6:7], s[6:7], s[10:11]
	v_cmp_eq_u32_e64 s[14:15], s44, v151
	s_and_b64 s[6:7], s[6:7], s[12:13]
	s_and_b64 s[6:7], s[6:7], s[14:15]
	v_cndmask_b32_e64 v141, 0, 1, s[6:7]
	v_cmp_ne_u32_e32 vcc, 0, v141
	s_mov_b64 s[6:7], -1
	s_cmp_eq_u64 vcc, exec
	s_mov_b64 s[8:9], -1
	s_cbranch_scc1 .LBB1_37
	s_and_b32 s6, s45, 0x3ff
	s_cmpk_eq_i32 s6, 0x3ff
	s_mov_b64 s[6:7], -1
	s_mov_b64 s[10:11], -1
	s_cbranch_scc0 .LBB1_42
	s_mov_b64 s[6:7], 0
	s_cmp_lt_u32 s45, 0x80001
	s_mov_b64 s[10:11], 0
	s_cbranch_scc0 .LBB1_42
	global_load_dword v141, v167, s[22:23] offset:4 sc1
	s_waitcnt vmcnt(0)
	v_cmp_eq_u32_e64 s[10:11], 0, v141

.LBB1_47:
	v_mov_b32_e32 v152, 0x44800000
	s_and_b32 s8, s44, 1
	v_cndmask_b32_e64 v152, v152, 0, s[4:5]
	s_mulk_i32 s8, 0x4200
	s_cmp_eq_u32 s43, 31
	s_cbranch_scc0 .Lpost_nosave
	v_mov_b32_e32 v202, v140
	v_mov_b32_e32 v198, v142
	v_mov_b32_e32 v197, v144
	v_mov_b32_e32 v196, v146
	v_mov_b32_e32 v179, v148
	v_mov_b32_e32 v177, v150
.Lpost_nosave:
	v_fma_mixlo_f16 v153, v140, v152, 0
	v_fma_mixhi_f16 v153, v142, v152, 0
	v_fma_mixlo_f16 v154, v144, v152, 0
	v_fma_mixhi_f16 v154, v146, v152, 0
	v_fma_mixlo_f16 v155, v148, v152, 0
	v_fma_mixhi_f16 v155, v150, v152, 0
	v_add_u32_e32 v156, s8, v231
	v_add_u32_e32 v157, s8, v232
	v_add_u32_e32 v158, s8, v233
	ds_write_b32 v156, v153
	ds_write_b32 v157, v154
	ds_write_b32 v158, v155
	s_andn2_b64 vcc, exec, s[38:39]
	s_cbranch_vccnz .LBB1_53
	v_fma_mixlo_f16 v159, v140, v152, -v153 op_sel_hi:[0,0,1]
	v_fma_mixhi_f16 v159, v142, v152, -v153 op_sel:[0,0,1] op_sel_hi:[0,0,1]
	v_fma_mixlo_f16 v160, v144, v152, -v154 op_sel_hi:[0,0,1]
	v_fma_mixhi_f16 v160, v146, v152, -v154 op_sel:[0,0,1] op_sel_hi:[0,0,1]
	v_fma_mixlo_f16 v161, v148, v152, -v155 op_sel_hi:[0,0,1]
	v_fma_mixhi_f16 v161, v150, v152, -v155 op_sel:[0,0,1] op_sel_hi:[0,0,1]
	ds_write_b32 v156, v159 offset:8448
	ds_write_b32 v157, v160 offset:8448
	ds_write_b32 v158, v161 offset:8448

.LBB1_55:
	s_xor_b64 s[10:11], s[10:11], -1
	s_lshl_b64 s[4:5], s[24:25], 15
	s_add_u32 s6, s18, s4
	s_addc_u32 s7, s19, s5
	s_waitcnt vmcnt(0)
	v_lshlrev_b32_e32 v130, 11, v171
	s_mov_b32 s4, 0
	v_mov_b32_e32 v131, 0
	v_lshl_add_u64 v[132:133], s[6:7], 0, v[130:131]
	s_lshl_b32 s6, s42, 3
	s_mov_b32 s7, s4
	v_lshl_add_u64 v[132:133], v[132:133], 0, s[6:7]
	v_lshlrev_b32_e32 v130, 3, v199
	s_cmp_gt_i32 s41, 0
	v_lshl_add_u64 v[132:133], v[132:133], 0, v[130:131]
	v_mov_b32_e32 v135, 1
	v_mov_b32_e32 v134, v188
	s_cselect_b64 s[8:9], -1, 0
	global_store_dwordx2 v[132:133], v[134:135], off sc1
	v_mov_b32_e32 v134, v189
	s_and_b64 s[12:13], s[8:9], exec
	global_store_dwordx2 v[132:133], v[134:135], off offset:32 sc1
	s_cselect_b32 s5, 15, 0
	v_add_co_u32_e32 v133, vcc, -1, v171
	v_mov_b32_e32 v132, s5
	s_or_b64 s[8:9], vcc, s[8:9]
	v_cndmask_b32_e32 v132, v132, v133, vcc
	v_mov_b32_e32 v133, s24
	s_xor_b64 vcc, vcc, s[8:9]
	v_subbrev_co_u32_e32 v134, vcc, 0, v133, vcc
	v_ashrrev_i32_e32 v135, 31, v134
	v_lshlrev_b64 v[136:137], 16, v[134:135]
	v_lshl_add_u64 v[136:137], s[16:17], 0, v[136:137]
	v_ashrrev_i32_e32 v133, 31, v132
	v_lshlrev_b32_e32 v138, 5, v132
	v_mov_b32_e32 v139, 0
	v_lshl_add_u64 v[136:137], v[136:137], 0, v[138:139]
	v_mov_b32_e32 v139, 0
	v_lshlrev_b32_e32 v208, 5, v171
	v_sub_u32_e32 v138, v228, v208
	v_lshl_add_u64 v[140:141], v[136:137], 0, v[138:139]
	v_sub_u32_e32 v138, v229, v208
	v_lshl_add_u64 v[144:145], v[136:137], 0, v[138:139]
	v_sub_u32_e32 v138, v230, v208
	v_lshl_add_u64 v[148:149], v[136:137], 0, v[138:139]
	v_lshlrev_b64 v[134:135], 15, v[134:135]
	v_lshl_add_u64 v[134:135], s[18:19], 0, v[134:135]
	v_lshlrev_b64 v[132:133], 11, v[132:133]
	v_lshl_add_u64 v[132:133], v[134:135], 0, v[132:133]
	v_lshl_add_u64 v[132:133], v[132:133], 0, s[6:7]
	v_lshl_add_u64 v[152:153], v[132:133], 0, v[130:131]
	v_mov_b32_e32 v208, 0
	v_mov_b32_e32 v210, 0
	v_mov_b32_e32 v212, 0
	v_mov_b32_e32 v214, 0
	v_mov_b32_e32 v216, 0
	v_mov_b32_e32 v218, 0
	v_mov_b32_e32 v220, 0
	v_mov_b32_e32 v222, 0
	s_mov_b32 s12, 1
	s_andn2_b64 vcc, exec, s[10:11]
	s_cbranch_vccnz .Lep_check
	s_mov_b32 s7, 0
.Lep_poll:
	global_load_dwordx4 v[208:211], v[140:141], off sc1
	global_load_dwordx4 v[212:215], v[144:145], off sc1
	global_load_dwordx4 v[216:219], v[148:149], off sc1
	global_load_dwordx2 v[220:221], v[152:153], off sc1
	global_load_dwordx2 v[222:223], v[152:153], off offset:32 sc1
	s_waitcnt vmcnt(0)
	v_cmp_eq_u32_e32 vcc, 36, v209
	v_cmp_eq_u32_e64 s[14:15], 36, v211
	v_cmp_eq_u32_e64 s[16:17], 36, v213
	s_and_b64 vcc, vcc, s[14:15]
	v_cmp_eq_u32_e64 s[14:15], 36, v215
	s_and_b64 vcc, vcc, s[16:17]
	v_cmp_eq_u32_e64 s[16:17], 36, v217
	s_and_b64 vcc, vcc, s[14:15]
	v_cmp_eq_u32_e64 s[14:15], 36, v219
	s_and_b64 vcc, vcc, s[16:17]
	v_cmp_eq_u32_e64 s[16:17], 1, v221
	s_and_b64 vcc, vcc, s[14:15]
	v_cmp_eq_u32_e64 s[14:15], 1, v223
	s_and_b64 vcc, vcc, s[16:17]
	s_and_b64 vcc, vcc, s[14:15]
	s_cmp_eq_u64 vcc, exec
	s_cbranch_scc1 .Lep_ok
	s_add_i32 s7, s7, 1
	s_and_b32 s13, s7, 0x3ff
	s_cmp_lg_u32 s13, 0
	s_cbranch_scc1 .Lep_poll
	s_cmp_gt_u32 s7, 0x80000
	s_cbranch_scc1 .Lep_dead
	v_mov_b32_e32 v138, 0
	global_load_dword v139, v138, s[22:23] offset:4 sc1
	s_waitcnt vmcnt(0)
	v_cmp_eq_u32_e64 s[14:15], 0, v139
	s_and_b64 vcc, exec, s[14:15]
	s_cbranch_vccnz .Lep_poll
